# v5 plus P10 next-unit queue claim issued before the epilogue (atomic latency under the epilogue)
# baseline (speedup 1.0000x reference)
.LBB0_1122:
	s_cmp_gt_i32 s28, 10
	s_cselect_b64 s[0:1], -1, 0
	s_cmp_lt_i32 s29, 11
	s_cselect_b64 s[6:7], -1, 0
	s_or_b64 s[0:1], s[0:1], s[6:7]
	s_and_b64 vcc, exec, s[0:1]
	s_cbranch_vccnz .LBB0_1244
	s_mov_b32 s99, 0
	v_cmp_gt_u32_e32 vcc, 64, v0
	s_and_saveexec_b64 s[6:7], vcc
	s_cbranch_execz .LBB0_1127
	s_waitcnt vmcnt(0)
	v_and_b32_e32 v1, 31, v0
	s_waitcnt lgkmcnt(0)
	v_lshlrev_b32_e32 v2, 7, v1
	global_load_dword v2, v2, s[26:27] offset:256 sc1
	v_mbcnt_lo_u32_b32 v3, -1, 0
	v_mbcnt_hi_u32_b32 v4, -1, v3
	v_and_b32_e32 v5, 0x60, v4
	v_add_u32_e32 v3, -1, v4
	v_cmp_lt_i32_e32 vcc, v3, v5
	v_add_u32_e32 v6, -2, v4
	v_add_u32_e32 v7, -4, v4
	v_cndmask_b32_e32 v3, v3, v4, vcc
	v_lshlrev_b32_e32 v9, 2, v3
	v_cmp_lt_i32_e32 vcc, v6, v5
	v_add_u32_e32 v8, -8, v4
	s_waitcnt vmcnt(0)
	v_add_u32_e32 v3, 0xff, v2
	v_lshrrev_b32_e32 v3, 8, v3
	ds_bpermute_b32 v9, v9, v3
	v_cndmask_b32_e32 v6, v6, v4, vcc
	v_cmp_ne_u32_e32 vcc, 0, v1
	v_lshlrev_b32_e32 v6, 2, v6
	s_waitcnt lgkmcnt(0)
	v_cndmask_b32_e32 v9, 0, v9, vcc
	v_add_u32_e32 v9, v9, v3
	ds_bpermute_b32 v6, v6, v9
	v_cmp_lt_i32_e32 vcc, v7, v5
	s_nop 1
	v_cndmask_b32_e32 v7, v7, v4, vcc
	v_cmp_lt_u32_e32 vcc, 1, v1
	v_lshlrev_b32_e32 v7, 2, v7
	s_waitcnt lgkmcnt(0)
	v_cndmask_b32_e32 v6, 0, v6, vcc
	v_add_u32_e32 v6, v6, v9
	ds_bpermute_b32 v7, v7, v6
	v_cmp_lt_i32_e32 vcc, v8, v5
	s_nop 1
	v_cndmask_b32_e32 v8, v8, v4, vcc
	v_cmp_lt_u32_e32 vcc, 3, v1
	v_lshlrev_b32_e32 v8, 2, v8
	s_waitcnt lgkmcnt(0)
	v_cndmask_b32_e32 v7, 0, v7, vcc
	v_add_u32_e32 v6, v7, v6
	ds_bpermute_b32 v7, v8, v6
	v_add_u32_e32 v8, -16, v4
	v_cmp_lt_i32_e32 vcc, v8, v5
	s_nop 1
	v_cndmask_b32_e32 v5, v8, v4, vcc
	v_cmp_lt_u32_e32 vcc, 7, v1
	v_lshlrev_b32_e32 v5, 2, v5
	s_waitcnt lgkmcnt(0)
	v_cndmask_b32_e32 v4, 0, v7, vcc
	v_add_u32_e32 v4, v4, v6
	ds_bpermute_b32 v5, v5, v4
	v_cmp_gt_u32_e32 vcc, 32, v0
	s_and_b64 exec, exec, vcc
	s_cbranch_execz .LBB0_1127
	v_cmp_lt_u32_e32 vcc, 15, v1
	s_waitcnt lgkmcnt(0)
	s_nop 0
	v_cndmask_b32_e32 v5, 0, v5, vcc
	v_add_u32_e32 v4, v5, v4
	v_lshl_add_u32 v5, v1, 2, 0
	v_add_u32_e32 v5, 0x23c00, v5
	v_cmp_eq_u32_e32 vcc, 31, v1
	v_sub_u32_e32 v1, v4, v3
	ds_write2_b32 v5, v1, v2 offset1:33
	s_and_b64 exec, exec, vcc
	s_add_i32 s3, 0, 0x23c80
	v_mov_b32_e32 v1, s3
	ds_write_b32 v1, v4

.LBB0_1152:
	s_add_i32 s90, s31, 1
	s_and_saveexec_b64 s[8:9], s[4:5]
	s_xor_b64 s[8:9], exec, s[8:9]
	s_and_b32 s34, s90, 1
	s_or_saveexec_b64 s[8:9], s[8:9]
	v_mov_b32_e32 v2, s34
	s_xor_b64 exec, exec, s[8:9]
	s_cbranch_execz .LBB0_1168
	v_mov_b32_e32 v2, s84
	ds_read2_b32 v[2:3], v2 offset1:4
	s_mov_b64 s[52:53], exec
	v_mbcnt_lo_u32_b32 v4, s52, 0
	v_mbcnt_hi_u32_b32 v4, s53, v4
	v_cmp_eq_u32_e32 vcc, 0, v4
	s_and_saveexec_b64 s[54:55], vcc
	s_cbranch_execz .LBB0_1157
	s_bcnt1_i32_b64 s18, s[52:53]
	s_cmp_lg_u32 s99, 0
	s_cbranch_scc1 .LBB0_1157
	v_mov_b32_e32 v244, s18
	global_atomic_add v244, v66, v244, s[12:13] sc0
.LBB0_1157:
	s_or_b64 exec, exec, s[54:55]
	s_waitcnt lgkmcnt(0)
	v_sub_u32_e32 v2, v3, v2
	s_waitcnt vmcnt(0)
	v_readfirstlane_b32 s18, v244
	s_mov_b32 s99, 0
	v_lshlrev_b32_e32 v2, 4, v2
	s_nop 0
	v_add_u32_e32 v3, s18, v4
	v_cmp_ge_u32_e32 vcc, v3, v2
	s_and_saveexec_b64 s[34:35], vcc
	s_xor_b64 s[52:53], exec, s[34:35]
	s_cbranch_execz .LBB0_1165
	s_mov_b32 s34, 1
	v_mov_b32_e32 v2, -1
	s_mov_b64 s[54:55], 0
	s_branch .LBB0_1161

.LBB0_1180:
	v_readlane_b32 s100, v252, 4
	v_readlane_b32 s101, v252, 5
	s_nop 3
	s_and_saveexec_b64 s[100:101], s[100:101]
	s_cbranch_execz .Lclaim_skip_p10
	v_mov_b32_e32 v244, 1
	global_atomic_add v244, v66, v244, s[12:13] sc0
.Lclaim_skip_p10:
	s_mov_b64 exec, s[100:101]
	s_mov_b32 s99, 1
	s_and_b64 vcc, exec, s[46:47]
	s_cbranch_vccz .LBB0_1182
	s_barrier
